# stream tail trimmed (select/address before the last row arrives); softmax hand-rewrite (energy loads first, interleaved max/sum reductions); on top of rotated wave-row + prep rewrite
# speedup vs baseline: 1.0075x; 1.0075x over previous
.LBB1_2:
	s_or_b64 exec, exec, s[0:1]
	s_lshr_b32 s8, s3, 6
	s_add_i32 s8, s8, s2
	s_and_b32 s8, s8, 15
	s_lshl_b32 s0, s2, 7
	v_and_b32_e32 v24, 63, v0
	s_add_i32 s9, s8, s0
	s_waitcnt lgkmcnt(0)
	s_and_b32 s1, s5, 0xffff
	s_mov_b32 s3, 0x20000
	s_brev_b32 s2, 16
	s_mov_b32 s0, s4
	v_lshlrev_b32_e32 v25, 4, v24
	s_lshl_b32 s4, s9, 12
	buffer_load_dwordx4 v[26:29], v25, s[0:3], s4 offen offset:1024 nt
	buffer_load_dwordx4 v[30:33], v25, s[0:3], s4 offen nt
	buffer_load_dwordx4 v[34:37], v25, s[0:3], s4 offen offset:2048 nt
	s_add_i32 s5, s4, 0x10000
	buffer_load_dwordx4 v[38:41], v25, s[0:3], s5 offen offset:1024 nt
	buffer_load_dwordx4 v[42:45], v25, s[0:3], s5 offen nt
	buffer_load_dwordx4 v[16:19], v25, s[0:3], s4 offen offset:3072 nt
	s_add_i32 s10, s4, 0x20000
	buffer_load_dwordx4 v[46:49], v25, s[0:3], s5 offen offset:2048 nt
	buffer_load_dwordx4 v[20:23], v25, s[0:3], s5 offen offset:3072 nt
	s_barrier
	buffer_load_dwordx4 v[50:53], v25, s[0:3], s10 offen offset:1024 nt
	buffer_load_dwordx4 v[54:57], v25, s[0:3], s10 offen nt
	ds_read_b128 v[4:7], v25 offset:1024
	ds_read_b128 v[0:3], v25
	ds_read_b128 v[12:15], v25 offset:2048
	ds_read_b128 v[8:11], v25 offset:3072
	s_add_i32 s5, s4, 0x30000
	v_cmp_gt_u32_e32 vcc, 8, v24
	s_waitcnt vmcnt(9) lgkmcnt(3)
	v_pk_mul_f32 v[28:29], v[6:7], v[28:29]
	v_pk_mul_f32 v[26:27], v[4:5], v[26:27]
	s_waitcnt vmcnt(8) lgkmcnt(2)
	v_pk_fma_f32 v[32:33], v[2:3], v[32:33], v[28:29]
	v_pk_fma_f32 v[30:31], v[0:1], v[30:31], v[26:27]
	buffer_load_dwordx4 v[26:29], v25, s[0:3], s5 offen offset:1024 nt
	s_waitcnt vmcnt(8) lgkmcnt(1)
	v_pk_fma_f32 v[58:59], v[14:15], v[36:37], v[32:33]
	v_pk_fma_f32 v[60:61], v[12:13], v[34:35], v[30:31]
	buffer_load_dwordx4 v[30:33], v25, s[0:3], s5 offen nt
	s_waitcnt vmcnt(8)
	v_pk_mul_f32 v[34:35], v[6:7], v[40:41]
	v_pk_mul_f32 v[36:37], v[4:5], v[38:39]
	s_waitcnt vmcnt(7)
	v_pk_fma_f32 v[44:45], v[2:3], v[44:45], v[34:35]
	v_pk_fma_f32 v[42:43], v[0:1], v[42:43], v[36:37]
	buffer_load_dwordx4 v[34:37], v25, s[0:3], s10 offen offset:2048 nt
	s_waitcnt vmcnt(4)
	v_pk_mul_f32 v[38:39], v[6:7], v[52:53]
	v_pk_mul_f32 v[40:41], v[4:5], v[50:51]
	s_waitcnt vmcnt(3)
	v_pk_fma_f32 v[50:51], v[2:3], v[56:57], v[38:39]
	v_pk_fma_f32 v[52:53], v[0:1], v[54:55], v[40:41]
	buffer_load_dwordx4 v[38:41], v25, s[0:3], s10 offen offset:3072 nt
	v_pk_fma_f32 v[48:49], v[14:15], v[48:49], v[44:45]
	v_pk_fma_f32 v[46:47], v[12:13], v[46:47], v[42:43]
	s_waitcnt lgkmcnt(0)
	v_pk_fma_f32 v[18:19], v[10:11], v[18:19], v[58:59]
	v_pk_fma_f32 v[16:17], v[8:9], v[16:17], v[60:61]
	v_add_f32_e32 v61, v18, v19
	v_add_f32_e32 v60, v16, v17
	v_pk_fma_f32 v[16:17], v[10:11], v[22:23], v[48:49]
	v_pk_fma_f32 v[18:19], v[8:9], v[20:21], v[46:47]
	v_add_f32_e32 v16, v16, v17
	v_add_f32_e32 v18, v18, v19
	v_add_f32_e32 v60, v60, v61
	v_add_f32_e32 v16, v18, v16
	s_add_i32 s10, s4, 0x50000
	s_waitcnt vmcnt(3)
	v_pk_mul_f32 v[28:29], v[6:7], v[28:29]
	v_pk_mul_f32 v[26:27], v[4:5], v[26:27]
	v_add_f32_dpp v16, v16, v16 quad_perm:[1,0,3,2] row_mask:0xf bank_mask:0xf bound_ctrl:1
	s_waitcnt vmcnt(2)
	v_pk_fma_f32 v[54:55], v[2:3], v[32:33], v[28:29]
	v_pk_fma_f32 v[56:57], v[0:1], v[30:31], v[26:27]
	buffer_load_dwordx4 v[26:29], v25, s[0:3], s5 offen offset:2048 nt
	buffer_load_dwordx4 v[30:33], v25, s[0:3], s5 offen offset:3072 nt
	s_add_i32 s5, s4, 0x40000
	buffer_load_dwordx4 v[42:45], v25, s[0:3], s5 offen offset:1024 nt
	s_waitcnt vmcnt(4)
	v_pk_fma_f32 v[50:51], v[14:15], v[36:37], v[50:51]
	v_pk_fma_f32 v[52:53], v[12:13], v[34:35], v[52:53]
	buffer_load_dwordx4 v[34:37], v25, s[0:3], s5 offen nt
	v_add_f32_dpp v16, v16, v16 quad_perm:[2,3,0,1] row_mask:0xf bank_mask:0xf bound_ctrl:1
	s_waitcnt vmcnt(4)
	v_pk_fma_f32 v[58:59], v[10:11], v[40:41], v[50:51]
	v_pk_fma_f32 v[38:39], v[8:9], v[38:39], v[52:53]
	v_add_f32_e32 v19, v58, v59
	v_add_f32_e32 v17, v38, v39
	v_add_f32_dpp v58, v60, v60 quad_perm:[1,0,3,2] row_mask:0xf bank_mask:0xf bound_ctrl:1
	v_add_f32_e32 v18, v17, v19
	v_add_f32_dpp v16, v16, v16 row_ror:4 row_mask:0xf bank_mask:0xf bound_ctrl:1
	v_add_f32_dpp v17, v58, v58 quad_perm:[2,3,0,1] row_mask:0xf bank_mask:0xf bound_ctrl:1
	buffer_load_dwordx4 v[20:23], v25, s[0:3], s5 offen offset:2048 nt
	buffer_load_dwordx4 v[46:49], v25, s[0:3], s5 offen offset:3072 nt
	v_add_f32_dpp v17, v17, v17 row_ror:4 row_mask:0xf bank_mask:0xf bound_ctrl:1
	v_add_f32_dpp v58, v16, v16 row_ror:8 row_mask:0xf bank_mask:0xf bound_ctrl:1
	buffer_load_dwordx4 v[38:41], v25, s[0:3], s10 offen nt
	buffer_load_dwordx4 v[50:53], v25, s[0:3], s10 offen offset:1024 nt
	v_add_f32_dpp v17, v17, v17 row_ror:8 row_mask:0xf bank_mask:0xf bound_ctrl:1
	v_mov_b32_e32 v19, v17
	v_mov_b32_e32 v59, v58
	s_nop 0
	v_permlane16_swap_b32_e32 v17, v19
	v_permlane16_swap_b32_e32 v58, v59
	v_add_f32_e32 v16, v17, v19
	v_add_f32_e32 v17, v58, v59
	s_add_i32 s5, s4, 0x60000
	s_add_i32 s4, s4, 0x70000
	v_add_f32_dpp v18, v18, v18 quad_perm:[1,0,3,2] row_mask:0xf bank_mask:0xf bound_ctrl:1
	s_waitcnt vmcnt(7)
	v_pk_fma_f32 v[28:29], v[14:15], v[28:29], v[54:55]
	v_pk_fma_f32 v[54:55], v[12:13], v[26:27], v[56:57]
	s_waitcnt vmcnt(6)
	v_pk_fma_f32 v[58:59], v[10:11], v[32:33], v[28:29]
	buffer_load_dwordx4 v[26:29], v25, s[0:3], s10 offen offset:2048 nt
	v_pk_fma_f32 v[54:55], v[8:9], v[30:31], v[54:55]
	buffer_load_dwordx4 v[30:33], v25, s[0:3], s10 offen offset:3072 nt
	v_add_f32_e32 v66, v54, v55
	s_waitcnt vmcnt(7)
	v_pk_mul_f32 v[54:55], v[6:7], v[44:45]
	v_pk_mul_f32 v[56:57], v[4:5], v[42:43]
	buffer_load_dwordx4 v[42:45], v25, s[0:3], s5 offen offset:1024 nt
	s_waitcnt vmcnt(7)
	v_pk_fma_f32 v[54:55], v[2:3], v[36:37], v[54:55]
	v_pk_fma_f32 v[56:57], v[0:1], v[34:35], v[56:57]
	buffer_load_dwordx4 v[34:37], v25, s[0:3], s5 offen nt
	v_add_f32_dpp v18, v18, v18 quad_perm:[2,3,0,1] row_mask:0xf bank_mask:0xf bound_ctrl:1
	s_waitcnt vmcnt(7)
	v_pk_fma_f32 v[22:23], v[14:15], v[22:23], v[54:55]
	v_pk_fma_f32 v[20:21], v[12:13], v[20:21], v[56:57]
	s_waitcnt vmcnt(6)
	v_pk_fma_f32 v[60:61], v[10:11], v[48:49], v[22:23]
	v_pk_fma_f32 v[22:23], v[8:9], v[46:47], v[20:21]
	s_waitcnt vmcnt(4)
	v_pk_mul_f32 v[54:55], v[4:5], v[50:51]
	v_pk_mul_f32 v[20:21], v[6:7], v[52:53]
	v_pk_fma_f32 v[38:39], v[0:1], v[38:39], v[54:55]
	buffer_load_dwordx4 v[46:49], v25, s[0:3], s5 offen offset:2048 nt
	buffer_load_dwordx4 v[50:53], v25, s[0:3], s5 offen offset:3072 nt
	v_pk_fma_f32 v[20:21], v[2:3], v[40:41], v[20:21]
	v_add_f32_e32 v23, v22, v23
	v_add_f32_dpp v18, v18, v18 row_ror:4 row_mask:0xf bank_mask:0xf bound_ctrl:1
	s_waitcnt vmcnt(5)
	v_pk_fma_f32 v[26:27], v[12:13], v[26:27], v[38:39]
	buffer_load_dwordx4 v[38:41], v25, s[0:3], s4 offen nt
	buffer_load_dwordx4 v[54:57], v25, s[0:3], s4 offen offset:1024 nt
	v_pk_fma_f32 v[20:21], v[14:15], v[28:29], v[20:21]
	s_waitcnt vmcnt(6)
	v_pk_fma_f32 v[30:31], v[8:9], v[30:31], v[26:27]
	v_pk_fma_f32 v[62:63], v[10:11], v[32:33], v[20:21]
	v_add_f32_dpp v18, v18, v18 row_ror:8 row_mask:0xf bank_mask:0xf bound_ctrl:1
	s_waitcnt vmcnt(5)
	v_pk_mul_f32 v[20:21], v[6:7], v[44:45]
	v_pk_mul_f32 v[26:27], v[4:5], v[42:43]
	buffer_load_dwordx4 v[42:45], v25, s[0:3], s4 offen offset:2048 nt
	s_waitcnt vmcnt(5)
	v_pk_fma_f32 v[64:65], v[0:1], v[34:35], v[26:27]
	buffer_load_dwordx4 v[32:35], v25, s[0:3], s4 offen offset:3072 nt
	v_add_f32_e32 v27, v60, v61
	v_add_f32_e32 v23, v23, v27
	v_pk_fma_f32 v[36:37], v[2:3], v[36:37], v[20:21]
	v_add_f32_e32 v20, v58, v59
	v_add_f32_dpp v23, v23, v23 quad_perm:[1,0,3,2] row_mask:0xf bank_mask:0xf bound_ctrl:1
	v_add_f32_e32 v20, v66, v20
	v_mov_b32_e32 v19, v18
	v_add_f32_dpp v23, v23, v23 quad_perm:[2,3,0,1] row_mask:0xf bank_mask:0xf bound_ctrl:1
	v_add_f32_dpp v20, v20, v20 quad_perm:[1,0,3,2] row_mask:0xf bank_mask:0xf bound_ctrl:1
	v_permlane16_swap_b32_e32 v18, v19
	v_add_f32_dpp v23, v23, v23 row_ror:4 row_mask:0xf bank_mask:0xf bound_ctrl:1
	v_add_f32_dpp v20, v20, v20 quad_perm:[2,3,0,1] row_mask:0xf bank_mask:0xf bound_ctrl:1
	v_add_f32_e32 v18, v18, v19
	v_add_f32_dpp v23, v23, v23 row_ror:8 row_mask:0xf bank_mask:0xf bound_ctrl:1
	v_mov_b32_e32 v27, v23
	s_nop 1
	v_permlane16_swap_b32_e32 v23, v27
	v_add_f32_e32 v28, v23, v27
	v_add_f32_e32 v23, v30, v31
	s_waitcnt vmcnt(5)
	v_pk_fma_f32 v[30:31], v[14:15], v[48:49], v[36:37]
	v_pk_fma_f32 v[36:37], v[12:13], v[46:47], v[64:65]
	s_waitcnt vmcnt(4)
	v_pk_fma_f32 v[30:31], v[10:11], v[52:53], v[30:31]
	v_pk_fma_f32 v[36:37], v[8:9], v[50:51], v[36:37]
	v_add_f32_e32 v27, v62, v63
	v_add_f32_e32 v36, v36, v37
	v_add_f32_e32 v30, v30, v31
	v_add_f32_e32 v23, v23, v27
	v_add_f32_e32 v30, v36, v30
	v_add_f32_dpp v20, v20, v20 row_ror:4 row_mask:0xf bank_mask:0xf bound_ctrl:1
	v_add_f32_dpp v23, v23, v23 quad_perm:[1,0,3,2] row_mask:0xf bank_mask:0xf bound_ctrl:1
	v_add_f32_dpp v30, v30, v30 quad_perm:[1,0,3,2] row_mask:0xf bank_mask:0xf bound_ctrl:1
	v_add_f32_dpp v20, v20, v20 row_ror:8 row_mask:0xf bank_mask:0xf bound_ctrl:1
	v_add_f32_dpp v23, v23, v23 quad_perm:[2,3,0,1] row_mask:0xf bank_mask:0xf bound_ctrl:1
	v_add_f32_dpp v30, v30, v30 quad_perm:[2,3,0,1] row_mask:0xf bank_mask:0xf bound_ctrl:1
	v_mov_b32_e32 v21, v20
	v_add_f32_dpp v23, v23, v23 row_ror:4 row_mask:0xf bank_mask:0xf bound_ctrl:1
	v_add_f32_dpp v30, v30, v30 row_ror:4 row_mask:0xf bank_mask:0xf bound_ctrl:1
	v_permlane16_swap_b32_e32 v20, v21
	v_add_f32_dpp v23, v23, v23 row_ror:8 row_mask:0xf bank_mask:0xf bound_ctrl:1
	v_add_f32_dpp v30, v30, v30 row_ror:8 row_mask:0xf bank_mask:0xf bound_ctrl:1
	v_mov_b32_e32 v27, v23
	v_mov_b32_e32 v31, v30
	s_nop 0
	v_permlane16_swap_b32_e32 v23, v27
	v_permlane16_swap_b32_e32 v30, v31
	v_add_f32_e32 v21, v20, v21
	v_add_f32_e32 v23, v23, v27
	v_add_f32_e32 v30, v30, v31
	v_mov_b32_e32 v19, v16
	v_mov_b32_e32 v20, v17
	v_mov_b32_e32 v22, v18
	v_mov_b32_e32 v26, v21
	v_mov_b32_e32 v29, v28
	v_mov_b32_e32 v27, v23
	v_mov_b32_e32 v31, v30
	v_permlane32_swap_b32_e32 v16, v19
	v_permlane32_swap_b32_e32 v17, v20
	v_permlane32_swap_b32_e32 v18, v22
	v_permlane32_swap_b32_e32 v21, v26
	v_permlane32_swap_b32_e32 v28, v29
	v_permlane32_swap_b32_e32 v23, v27
	v_permlane32_swap_b32_e32 v30, v31
	v_add_f32_e32 v60, v16, v19
	v_cmp_eq_u32_e32 vcc, 0, v24
	v_add_f32_e32 v61, v17, v20
	v_add_f32_e32 v62, v18, v22
	v_cndmask_b32_e32 v60, 0, v60, vcc
	v_cmp_eq_u32_e32 vcc, 1, v24
	v_add_f32_e32 v63, v21, v26
	v_add_f32_e32 v64, v28, v29
	v_cndmask_b32_e32 v60, v60, v61, vcc
	v_cmp_eq_u32_e32 vcc, 2, v24
	v_add_f32_e32 v65, v23, v27
	v_add_f32_e32 v66, v30, v31
	v_cndmask_b32_e32 v60, v60, v62, vcc
	v_cmp_eq_u32_e32 vcc, 3, v24
	s_lshl_b32 s0, s8, 13
	s_lshr_b32 s1, s9, 4
	v_cndmask_b32_e32 v60, v60, v63, vcc
	v_cmp_eq_u32_e32 vcc, 4, v24
	s_lshl_b32 s1, s1, 2
	s_add_i32 s0, s0, s1
	v_cndmask_b32_e32 v60, v60, v64, vcc
	v_cmp_eq_u32_e32 vcc, 5, v24
	s_addk_i32 s0, 0x6040
	s_nop 0
	v_cndmask_b32_e32 v60, v60, v65, vcc
	v_cmp_eq_u32_e32 vcc, 6, v24
	v_lshl_add_u32 v61, v24, 2, s0
	s_nop 0
	v_cndmask_b32_e32 v60, v60, v66, vcc
	v_cmp_gt_u32_e64 s[2:3], 8, v24
	v_cmp_eq_u32_e32 vcc, 7, v24
	s_waitcnt vmcnt(2)
	v_pk_mul_f32 v[6:7], v[6:7], v[56:57]
	v_pk_mul_f32 v[4:5], v[4:5], v[54:55]
	v_pk_fma_f32 v[2:3], v[2:3], v[40:41], v[6:7]
	v_pk_fma_f32 v[0:1], v[0:1], v[38:39], v[4:5]
	s_waitcnt vmcnt(1)
	v_pk_fma_f32 v[2:3], v[14:15], v[44:45], v[2:3]
	v_pk_fma_f32 v[0:1], v[12:13], v[42:43], v[0:1]
	s_waitcnt vmcnt(0)
	v_pk_fma_f32 v[2:3], v[10:11], v[34:35], v[2:3]
	v_pk_fma_f32 v[0:1], v[8:9], v[32:33], v[0:1]
	s_nop 0
	v_add_f32_e32 v0, v0, v1
	v_add_f32_e32 v1, v2, v3
	v_add_f32_e32 v0, v0, v1
	s_nop 1
	v_add_f32_dpp v0, v0, v0 quad_perm:[1,0,3,2] row_mask:0xf bank_mask:0xf bound_ctrl:1
	s_nop 1
	v_add_f32_dpp v0, v0, v0 quad_perm:[2,3,0,1] row_mask:0xf bank_mask:0xf bound_ctrl:1
	s_nop 1
	v_add_f32_dpp v0, v0, v0 row_ror:4 row_mask:0xf bank_mask:0xf bound_ctrl:1
	s_nop 1
	v_add_f32_dpp v0, v0, v0 row_ror:8 row_mask:0xf bank_mask:0xf bound_ctrl:1
	v_mov_b32_e32 v1, v0
	s_nop 1
	v_permlane16_swap_b32_e32 v0, v1
	v_add_f32_e32 v0, v0, v1
	v_mov_b32_e32 v1, v0
	s_nop 1
	v_permlane32_swap_b32_e32 v0, v1
	v_add_f32_e32 v0, v0, v1
	v_cndmask_b32_e32 v60, v60, v0, vcc
	s_and_saveexec_b64 s[0:1], s[2:3]
	global_store_dword v61, v60, s[6:7]
	s_endpgm

_Z14softmax_kernelPKfPf:
	s_load_dwordx4 s[4:7], s[0:1], 0x0
	v_and_b32_e32 v1, 63, v0
	v_lshlrev_b32_e32 v2, 4, v0
	v_add_u32_e32 v3, 0x1000, v2
	s_lshl_b32 s8, s2, 13
	s_add_i32 s9, s8, 0x6040
	s_lshl_b32 s10, s2, 2
	s_add_i32 s10, s10, 0x4000
	v_lshl_add_u32 v16, v1, 6, s10
	v_add_u32_e32 v17, 0x1000, v16
	v_lshrrev_b32_e32 v20, 6, v0
	v_lshlrev_b32_e32 v20, 2, v20
	v_mov_b32_e32 v21, 0
	s_waitcnt lgkmcnt(0)
	s_add_u32 s12, s4, s9
	s_addc_u32 s13, s5, 0
	global_load_dwordx4 v[4:7], v2, s[12:13]
	global_load_dwordx4 v[8:11], v3, s[12:13]
	global_load_dword v12, v16, s[4:5]
	global_load_dword v13, v17, s[4:5]
	s_load_dword s16, s[4:5], 0x6000
	s_add_u32 s14, s6, s8
	s_addc_u32 s15, s7, 0
	v_cmp_eq_u32_e32 vcc, 0, v1
	s_waitcnt vmcnt(2)
	v_max3_f32 v14, v4, v5, v6
	v_max3_f32 v15, v7, v8, v9
	v_max3_f32 v14, v14, v10, v11
	s_nop 0
	v_max_f32_e32 v14, v14, v15
	s_waitcnt vmcnt(0)
	v_add_f32_e32 v12, v12, v13
	s_nop 0
	v_max_f32_dpp v14, v14, v14 quad_perm:[1,0,3,2] row_mask:0xf bank_mask:0xf bound_ctrl:1
	s_nop 0
	v_add_f32_dpp v12, v12, v12 quad_perm:[1,0,3,2] row_mask:0xf bank_mask:0xf bound_ctrl:1
	s_nop 0
	v_max_f32_dpp v14, v14, v14 quad_perm:[2,3,0,1] row_mask:0xf bank_mask:0xf bound_ctrl:1
	s_nop 0
	v_add_f32_dpp v12, v12, v12 quad_perm:[2,3,0,1] row_mask:0xf bank_mask:0xf bound_ctrl:1
	s_nop 0
	v_max_f32_dpp v14, v14, v14 row_ror:4 row_mask:0xf bank_mask:0xf bound_ctrl:1
	s_nop 0
	v_add_f32_dpp v12, v12, v12 row_ror:4 row_mask:0xf bank_mask:0xf bound_ctrl:1
	s_nop 0
	v_max_f32_dpp v14, v14, v14 row_ror:8 row_mask:0xf bank_mask:0xf bound_ctrl:1
	s_nop 0
	v_add_f32_dpp v12, v12, v12 row_ror:8 row_mask:0xf bank_mask:0xf bound_ctrl:1
	v_mov_b32_e32 v15, v14
	v_mov_b32_e32 v13, v12
	s_nop 1
	v_permlane16_swap_b32_e32 v14, v15
	v_permlane16_swap_b32_e32 v12, v13
	v_max_f32_e32 v14, v14, v15
	v_add_f32_e32 v12, v12, v13
	v_mov_b32_e32 v15, v14
	v_mov_b32_e32 v13, v12
	s_nop 1
	v_permlane32_swap_b32_e32 v14, v15
	v_permlane32_swap_b32_e32 v12, v13
	v_max_f32_e32 v14, v14, v15
	v_add_f32_e32 v12, v12, v13
	s_and_saveexec_b64 s[18:19], vcc
	ds_write_b32 v20, v14
	s_mov_b64 exec, s[18:19]
	s_waitcnt lgkmcnt(0)
	s_barrier
	ds_read_b128 v[22:25], v21
	v_add_f32_e32 v12, s16, v12
	v_pk_add_f32 v[4:5], v[4:5], v[12:13] op_sel_hi:[1,0]
	v_pk_add_f32 v[6:7], v[6:7], v[12:13] op_sel_hi:[1,0]
	v_pk_add_f32 v[8:9], v[8:9], v[12:13] op_sel_hi:[1,0]
	v_pk_add_f32 v[10:11], v[10:11], v[12:13] op_sel_hi:[1,0]
	s_waitcnt lgkmcnt(0)
	v_max_f32_e32 v22, v22, v23
	v_max3_f32 v22, v22, v24, v25
	v_add_f32_e32 v22, v22, v12
	v_sub_f32_e32 v4, v4, v22
	v_sub_f32_e32 v5, v5, v22
	v_sub_f32_e32 v6, v6, v22
	v_sub_f32_e32 v7, v7, v22
	v_sub_f32_e32 v8, v8, v22
	v_sub_f32_e32 v9, v9, v22
	v_sub_f32_e32 v10, v10, v22
	v_sub_f32_e32 v11, v11, v22
	v_mul_f32_e32 v4, 0x3fb8aa3b, v4
	v_mul_f32_e32 v5, 0x3fb8aa3b, v5
	v_mul_f32_e32 v6, 0x3fb8aa3b, v6
	v_mul_f32_e32 v7, 0x3fb8aa3b, v7
	v_mul_f32_e32 v8, 0x3fb8aa3b, v8
	v_mul_f32_e32 v9, 0x3fb8aa3b, v9
	v_mul_f32_e32 v10, 0x3fb8aa3b, v10
	v_mul_f32_e32 v11, 0x3fb8aa3b, v11
	v_exp_f32_e32 v4, v4
	v_exp_f32_e32 v5, v5
	v_exp_f32_e32 v6, v6
	v_exp_f32_e32 v7, v7
	v_exp_f32_e32 v8, v8
	v_exp_f32_e32 v9, v9
	v_exp_f32_e32 v10, v10
	v_exp_f32_e32 v11, v11
	v_add_f32_e32 v26, v4, v5
	v_add_f32_e32 v27, v6, v7
	v_add_f32_e32 v28, v8, v9
	s_nop 0
	v_add_f32_e32 v29, v10, v11
	v_add_f32_e32 v26, v26, v27
	v_add_f32_e32 v28, v28, v29
	v_add_f32_e32 v26, v26, v28
	s_nop 1
	v_add_f32_dpp v26, v26, v26 quad_perm:[1,0,3,2] row_mask:0xf bank_mask:0xf bound_ctrl:1
	s_nop 1
	v_add_f32_dpp v26, v26, v26 quad_perm:[2,3,0,1] row_mask:0xf bank_mask:0xf bound_ctrl:1
	s_nop 1
	v_add_f32_dpp v26, v26, v26 row_ror:4 row_mask:0xf bank_mask:0xf bound_ctrl:1
	s_nop 1
	v_add_f32_dpp v26, v26, v26 row_ror:8 row_mask:0xf bank_mask:0xf bound_ctrl:1
	v_mov_b32_e32 v27, v26
	s_nop 1
	v_permlane16_swap_b32_e32 v26, v27
	v_add_f32_e32 v26, v26, v27
	v_mov_b32_e32 v27, v26
	s_nop 1
	v_permlane32_swap_b32_e32 v26, v27
	v_add_f32_e32 v26, v26, v27
	s_and_saveexec_b64 s[18:19], vcc
	ds_write_b32 v20, v26 offset:16
	s_mov_b64 exec, s[18:19]
	s_waitcnt lgkmcnt(0)
	s_barrier
	ds_read_b128 v[22:25], v21 offset:16
	s_waitcnt lgkmcnt(0)
	v_add_f32_e32 v22, v22, v23
	v_add_f32_e32 v24, v24, v25
	v_add_f32_e32 v22, v22, v24
	v_div_scale_f32 v23, s[2:3], v22, v22, 1.0
	v_rcp_f32_e32 v24, v23
	v_div_scale_f32 v25, vcc, 1.0, v22, 1.0
	v_fma_f32 v26, -v23, v24, 1.0
	v_fmac_f32_e32 v24, v26, v24
	v_mul_f32_e32 v26, v25, v24
	v_fma_f32 v27, -v23, v26, v25
	v_fmac_f32_e32 v26, v27, v24
	v_fma_f32 v23, -v23, v26, v25
	v_div_fmas_f32 v23, v23, v24, v26
	v_div_fixup_f32 v26, v23, v22, 1.0
	v_pk_mul_f32 v[4:5], v[4:5], v[26:27] op_sel_hi:[1,0]
	v_pk_mul_f32 v[6:7], v[6:7], v[26:27] op_sel_hi:[1,0]
	v_pk_mul_f32 v[8:9], v[8:9], v[26:27] op_sel_hi:[1,0]
	v_pk_mul_f32 v[10:11], v[10:11], v[26:27] op_sel_hi:[1,0]
	global_store_dwordx4 v2, v[4:7], s[14:15]
	global_store_dwordx4 v3, v[8:11], s[14:15]
	s_endpgm

	.amdhsa_kernel _Z14softmax_kernelPKfPf
		.amdhsa_group_segment_fixed_size 32
		.amdhsa_private_segment_fixed_size 0
		.amdhsa_kernarg_size 16
		.amdhsa_user_sgpr_count 2
		.amdhsa_user_sgpr_dispatch_ptr 0
		.amdhsa_user_sgpr_queue_ptr 0
		.amdhsa_user_sgpr_kernarg_segment_ptr 1
		.amdhsa_user_sgpr_dispatch_id 0
		.amdhsa_user_sgpr_kernarg_preload_length 0
		.amdhsa_user_sgpr_kernarg_preload_offset 0
		.amdhsa_user_sgpr_private_segment_size 0
		.amdhsa_uses_dynamic_stack 0
		.amdhsa_enable_private_segment 0
		.amdhsa_system_sgpr_workgroup_id_x 1
		.amdhsa_system_sgpr_workgroup_id_y 0
		.amdhsa_system_sgpr_workgroup_id_z 0
		.amdhsa_system_sgpr_workgroup_info 0
		.amdhsa_system_vgpr_workitem_id 0
		.amdhsa_next_free_vgpr 32
		.amdhsa_next_free_sgpr 20
		.amdhsa_accum_offset 32
		.amdhsa_reserve_vcc 1
		.amdhsa_float_round_mode_32 0
		.amdhsa_float_round_mode_16_64 0
		.amdhsa_float_denorm_mode_32 3
		.amdhsa_float_denorm_mode_16_64 3
		.amdhsa_dx10_clamp 1
		.amdhsa_ieee_mode 1
		.amdhsa_fp16_overflow 0
		.amdhsa_tg_split 0
		.amdhsa_exception_fp_ieee_invalid_op 0
		.amdhsa_exception_fp_denorm_src 0
		.amdhsa_exception_fp_ieee_div_zero 0
		.amdhsa_exception_fp_ieee_overflow 0
		.amdhsa_exception_fp_ieee_underflow 0
		.amdhsa_exception_fp_ieee_inexact 0
		.amdhsa_exception_int_div_zero 0
	.end_amdhsa_kernel

.Lfunc_end2:
	.size	_Z14softmax_kernelPKfPf, .Lfunc_end2-_Z14softmax_kernelPKfPf
	.set _Z14softmax_kernelPKfPf.num_vgpr, 32
	.set _Z14softmax_kernelPKfPf.num_agpr, 0
	.set _Z14softmax_kernelPKfPf.numbered_sgpr, 20
	.set _Z14softmax_kernelPKfPf.num_named_barrier, 0
	.set _Z14softmax_kernelPKfPf.private_seg_size, 0
	.set _Z14softmax_kernelPKfPf.uses_vcc, 1
	.set _Z14softmax_kernelPKfPf.uses_flat_scratch, 0
	.set _Z14softmax_kernelPKfPf.has_dyn_sized_stack, 0
	.set _Z14softmax_kernelPKfPf.has_recursion, 0
	.set _Z14softmax_kernelPKfPf.has_indirect_call, 0

amdhsa.kernels:
  - .agpr_count:     0
    .args:
      - .actual_access:  read_only
        .address_space:  global
        .offset:         0
        .size:           8
        .value_kind:     global_buffer
      - .actual_access:  read_only
        .address_space:  global
        .offset:         8
        .size:           8
        .value_kind:     global_buffer
      - .actual_access:  read_only
        .address_space:  global
        .offset:         16
        .size:           8
        .value_kind:     global_buffer
      - .actual_access:  read_only
        .address_space:  global
        .offset:         24
        .size:           8
        .value_kind:     global_buffer
      - .actual_access:  write_only
        .address_space:  global
        .offset:         32
        .size:           8
        .value_kind:     global_buffer
    .group_segment_fixed_size: 2112
    .kernarg_segment_align: 8
    .kernarg_segment_size: 40
    .language:       OpenCL C
    .language_version:
      - 2
      - 0
    .max_flat_workgroup_size: 1024
    .name:           _Z11prep_kernelPKfS0_S0_S0_Pf
    .private_segment_fixed_size: 0
    .sgpr_count:     32
    .sgpr_spill_count: 0
    .symbol:         _Z11prep_kernelPKfS0_S0_S0_Pf.kd
    .uniform_work_group_size: 1
    .uses_dynamic_stack: false
    .vgpr_count:     40
    .vgpr_spill_count: 0
    .wavefront_size: 64
  - .agpr_count:     0
    .args:
      - .actual_access:  read_only
        .address_space:  global
        .offset:         0
        .size:           8
        .value_kind:     global_buffer
      - .address_space:  global
        .offset:         8
        .size:           8
        .value_kind:     global_buffer
    .group_segment_fixed_size: 4096
    .kernarg_segment_align: 8
    .kernarg_segment_size: 16
    .language:       OpenCL C
    .language_version:
      - 2
      - 0
    .max_flat_workgroup_size: 1024
    .name:           _Z13stream_kernelPKfPf
    .private_segment_fixed_size: 0
    .sgpr_count:     17
    .sgpr_spill_count: 0
    .symbol:         _Z13stream_kernelPKfPf.kd
    .uniform_work_group_size: 1
    .uses_dynamic_stack: false
    .vgpr_count:     67
    .vgpr_spill_count: 0
    .wavefront_size: 64
  - .agpr_count:     0
    .args:
      - .actual_access:  read_only
        .address_space:  global
        .offset:         0
        .size:           8
        .value_kind:     global_buffer
      - .actual_access:  write_only
        .address_space:  global
        .offset:         8
        .size:           8
        .value_kind:     global_buffer
    .group_segment_fixed_size: 32
    .kernarg_segment_align: 8
    .kernarg_segment_size: 16
    .language:       OpenCL C
    .language_version:
      - 2
      - 0
    .max_flat_workgroup_size: 256
    .name:           _Z14softmax_kernelPKfPf
    .private_segment_fixed_size: 0
    .sgpr_count:     26
    .sgpr_spill_count: 0
    .symbol:         _Z14softmax_kernelPKfPf.kd
    .uniform_work_group_size: 1
    .uses_dynamic_stack: false
    .vgpr_count:     32
    .vgpr_spill_count: 0
    .wavefront_size: 64
